# v15: v11 + P7 router bank-conflict-free LDS reads with 8 reads in flight, NSA ticket atomic wait deferred, scratch-store drains taken off two NSA barriers
# speedup vs baseline: 1.0135x; 1.0085x over previous
.LBB0_703:
	v_mov_b32_e32 v200, v3
	s_and_saveexec_b64 s[2:3], s[92:93]
	s_cbranch_execz .LBB0_707
	s_mov_b64 s[8:9], exec
	v_mbcnt_lo_u32_b32 v2, s8, 0
	v_mbcnt_hi_u32_b32 v2, s9, v2
	v_cmp_eq_u32_e32 vcc, 0, v2
	s_and_saveexec_b64 s[6:7], vcc
	s_cbranch_execz .LBB0_706
	s_bcnt1_i32_b64 s8, s[8:9]
	s_waitcnt vmcnt(23)
	v_mov_b32_e32 v4, s8
	v_readlane_b32 s8, v254, 54
	v_readlane_b32 s9, v254, 55
	s_nop 4
	global_atomic_add v200, v3, v4, s[8:9] sc0
.LBB0_706:
	s_or_b64 exec, exec, s[6:7]
.LBB0_707:
	s_or_b64 exec, exec, s[2:3]
	s_bitcmp1_b32 s10, 0
	s_cselect_b64 s[2:3], -1, 0
	s_ashr_i32 s18, s10, 1
	v_readlane_b32 s6, v254, 60
	s_cmp_lt_i32 s18, s6
	s_cselect_b64 s[6:7], -1, 0
	s_and_b64 s[2:3], s[2:3], s[6:7]
	s_andn2_b64 vcc, exec, s[2:3]
	s_mov_b64 s[2:3], -1
	s_cbranch_vccnz .LBB0_710
	s_and_b64 vcc, exec, s[2:3]
	s_cbranch_vccnz .LBB0_938

.LBB0_760:
	s_or_b64 exec, exec, s[2:3]
	s_add_i32 s2, s66, s94
	s_add_i32 s66, s2, s67
	v_lshlrev_b32_e32 v165, 12, v190
	s_lshl_b32 s2, s71, 9
	v_or3_b32 v166, v165, s2, v192
	s_lshr_b32 s2, s66, 5
	s_and_b32 s2, s2, 0x1fffe
	s_or_b32 s2, s2, s71
	s_lshl_b32 s2, s2, 15
	s_lshl_b32 s3, s68, 12
	v_mov_b32_e32 v2, v166
	s_add_i32 s2, s2, s3
	v_lshl_or_b32 v140, v206, 2, s2
	v_mov_b32_e32 v2, v140
	s_waitcnt lgkmcnt(0)
	v_add_u32_e32 v164, s6, v138
	ds_read_b128 v[68:71], v164
	ds_read_b128 v[72:75], v164 offset:32
	v_readlane_b32 s2, v255, 0
	v_readlane_b32 s3, v255, 1
	s_sub_i32 s7, 0x7d, s30
	s_waitcnt lgkmcnt(0)
	v_pk_mul_f32 v[20:21], v[20:21], v[68:69]
	v_pk_mul_f32 v[4:5], v[4:5], v[68:69]
	v_pk_mul_f32 v[52:53], v[52:53], v[68:69]
	v_pk_mul_f32 v[36:37], v[36:37], v[68:69]
	v_pk_mul_f32 v[22:23], v[22:23], v[70:71]
	v_pk_mul_f32 v[6:7], v[6:7], v[70:71]
	v_pk_mul_f32 v[54:55], v[54:55], v[70:71]
	v_pk_mul_f32 v[38:39], v[38:39], v[70:71]
	ds_read_b128 v[68:71], v164 offset:64
	v_pk_mul_f32 v[24:25], v[24:25], v[72:73]
	v_pk_mul_f32 v[8:9], v[8:9], v[72:73]
	v_pk_mul_f32 v[56:57], v[56:57], v[72:73]
	v_pk_mul_f32 v[40:41], v[40:41], v[72:73]
	v_pk_mul_f32 v[26:27], v[26:27], v[74:75]
	v_pk_mul_f32 v[10:11], v[10:11], v[74:75]
	v_pk_mul_f32 v[58:59], v[58:59], v[74:75]
	v_pk_mul_f32 v[42:43], v[42:43], v[74:75]
	ds_read_b128 v[72:75], v164 offset:96
	s_waitcnt lgkmcnt(0)
	v_pk_mul_f32 v[28:29], v[28:29], v[68:69]
	v_pk_mul_f32 v[12:13], v[12:13], v[68:69]
	v_pk_mul_f32 v[60:61], v[60:61], v[68:69]
	v_pk_mul_f32 v[44:45], v[44:45], v[68:69]
	v_lshl_add_u64 v[68:69], v[2:3], 2, s[2:3]
	s_movk_i32 s2, 0x1000
	v_pk_mul_f32 v[14:15], v[14:15], v[70:71]
	v_pk_mul_f32 v[16:17], v[16:17], v[72:73]
	v_pk_mul_f32 v[18:19], v[18:19], v[74:75]
	global_store_dwordx4 v[68:69], v[4:7], off
	global_store_dwordx4 v[68:69], v[8:11], off offset:1024
	global_store_dwordx4 v[68:69], v[12:15], off offset:2048
	global_store_dwordx4 v[68:69], v[16:19], off offset:3072
	v_add_co_u32_e32 v4, vcc, s2, v68
	s_movk_i32 s2, 0x2000
	s_nop 0
	v_addc_co_u32_e32 v5, vcc, 0, v69, vcc
	v_add_co_u32_e32 v6, vcc, s2, v68
	s_movk_i32 s2, 0x3000
	s_nop 0
	v_addc_co_u32_e32 v7, vcc, 0, v69, vcc
	s_max_i32 s3, s30, 0x7d
	v_pk_mul_f32 v[62:63], v[62:63], v[70:71]
	v_pk_mul_f32 v[46:47], v[46:47], v[70:71]
	v_pk_mul_f32 v[64:65], v[64:65], v[72:73]
	v_pk_mul_f32 v[48:49], v[48:49], v[72:73]
	v_pk_mul_f32 v[66:67], v[66:67], v[74:75]
	v_pk_mul_f32 v[50:51], v[50:51], v[74:75]
	global_store_dwordx4 v[6:7], v[52:55], off offset:-4096
	global_store_dwordx4 v[4:5], v[56:59], off offset:1024
	global_store_dwordx4 v[4:5], v[60:63], off offset:2048
	global_store_dwordx4 v[4:5], v[64:67], off offset:3072
	global_store_dwordx4 v[6:7], v[36:39], off
	global_store_dwordx4 v[6:7], v[40:43], off offset:1024
	global_store_dwordx4 v[6:7], v[44:47], off offset:2048
	global_store_dwordx4 v[6:7], v[48:51], off offset:3072
	v_add_co_u32_e32 v4, vcc, s2, v68
	s_max_i32 s2, s7, 0
	s_add_i32 s6, s3, 0xffffff90
	v_addc_co_u32_e32 v5, vcc, 0, v69, vcc
	s_cmp_gt_u32 s2, s6
	s_mov_b64 s[2:3], -1
	v_pk_mul_f32 v[30:31], v[30:31], v[70:71]
	v_pk_mul_f32 v[32:33], v[32:33], v[72:73]
	v_pk_mul_f32 v[34:35], v[34:35], v[74:75]
	global_store_dwordx4 v[4:5], v[20:23], off
	global_store_dwordx4 v[4:5], v[24:27], off offset:1024
	global_store_dwordx4 v[4:5], v[28:31], off offset:2048
	global_store_dwordx4 v[4:5], v[32:35], off offset:3072
	s_barrier
	s_cbranch_scc1 .LBB0_762
	s_max_i32 s2, s65, -1
	s_add_i32 s2, s2, 1
	s_min_u32 s2, s2, 32
	s_lshl_b32 s2, -1, s2
	s_not_b32 s2, s2
	s_cmpk_gt_i32 s30, 0x60
	s_cselect_b32 s12, s2, -1
	s_max_i32 s2, s65, 31
	s_sub_i32 s2, s2, 31
	s_min_u32 s2, s2, 32
	s_lshl_b32 s2, -1, s2
	s_not_b32 s2, s2
	s_cmp_gt_i32 s30, 64
	s_cselect_b32 s13, s2, -1
	s_max_i32 s2, s65, 63
	s_sub_i32 s2, s2, 63
	s_min_u32 s2, s2, 32
	s_lshl_b32 s2, -1, s2
	s_not_b32 s2, s2
	s_cmp_gt_i32 s30, 32
	s_cselect_b32 s14, s2, -1
	s_max_i32 s2, s65, 0x5f
	s_addk_i32 s2, 0xffa1
	s_min_u32 s2, s2, 32
	s_lshl_b32 s2, -1, s2
	s_not_b32 s2, s2
	s_cmp_gt_i32 s30, 0
	s_cselect_b32 s15, s2, -1
	s_mov_b64 s[2:3], 0

.LBB0_782:
	s_or_b64 exec, exec, s[2:3]
	v_mov_b32_e32 v2, v166
	v_readlane_b32 s2, v255, 0
	v_mov_b32_e32 v2, v140
	v_readlane_b32 s3, v255, 1
	s_waitcnt lgkmcnt(0)
	s_cmp_lt_i32 s64, 0
	s_nop 0
	v_lshl_add_u64 v[162:163], v[2:3], 2, s[2:3]
	v_add_co_u32_e32 v204, vcc, 0x1000, v162
	s_movk_i32 s2, 0x2000
	s_nop 0
	v_addc_co_u32_e32 v205, vcc, 0, v163, vcc
	v_add_co_u32_e32 v206, vcc, s2, v162
	global_load_dwordx4 v[68:71], v[162:163], off
	global_load_dwordx4 v[72:75], v[162:163], off offset:1024
	global_load_dwordx4 v[76:79], v[162:163], off offset:2048
	global_load_dwordx4 v[80:83], v[162:163], off offset:3072
	v_addc_co_u32_e32 v207, vcc, 0, v163, vcc
	s_movk_i32 s2, 0x3000
	v_add_co_u32_e32 v208, vcc, s2, v162
	global_load_dwordx4 v[84:87], v[204:205], off
	global_load_dwordx4 v[88:91], v[204:205], off offset:1024
	global_load_dwordx4 v[92:95], v[204:205], off offset:2048
	global_load_dwordx4 v[96:99], v[204:205], off offset:3072
	v_addc_co_u32_e32 v209, vcc, 0, v163, vcc
	global_load_dwordx4 v[132:135], v[208:209], off offset:-4096
	global_load_dwordx4 v[142:145], v[206:207], off offset:1024
	global_load_dwordx4 v[146:149], v[206:207], off offset:2048
	global_load_dwordx4 v[150:153], v[206:207], off offset:3072
	global_load_dwordx4 v[154:157], v[208:209], off
	global_load_dwordx4 v[158:161], v[208:209], off offset:1024
	global_load_dwordx4 v[168:171], v[208:209], off offset:2048
	global_load_dwordx4 v[172:175], v[208:209], off offset:3072
	ds_read_b128 v[176:179], v164
	ds_read_b128 v[180:183], v164 offset:32
	v_mov_b32_e32 v2, 0
	s_waitcnt vmcnt(0) lgkmcnt(0)
	v_pk_fma_f32 v[4:5], v[4:5], v[176:177], v[68:69]
	v_pk_fma_f32 v[6:7], v[6:7], v[178:179], v[70:71]
	ds_read_b128 v[68:71], v164 offset:64
	v_pk_fma_f32 v[8:9], v[8:9], v[180:181], v[72:73]
	v_pk_fma_f32 v[10:11], v[10:11], v[182:183], v[74:75]
	v_pk_fma_f32 v[38:39], v[38:39], v[178:179], v[134:135]
	v_pk_fma_f32 v[22:23], v[22:23], v[178:179], v[86:87]
	s_waitcnt lgkmcnt(0)
	v_pk_fma_f32 v[12:13], v[12:13], v[68:69], v[76:77]
	v_pk_fma_f32 v[14:15], v[14:15], v[70:71], v[78:79]
	v_pk_fma_f32 v[30:31], v[30:31], v[70:71], v[94:95]
	v_pk_fma_f32 v[28:29], v[28:29], v[68:69], v[92:93]
	v_pk_fma_f32 v[46:47], v[46:47], v[70:71], v[148:149]
	v_pk_fma_f32 v[44:45], v[44:45], v[68:69], v[146:147]
	v_pk_fma_f32 v[62:63], v[62:63], v[70:71], v[170:171]
	v_pk_fma_f32 v[60:61], v[60:61], v[68:69], v[168:169]
	ds_read_b128 v[68:71], v164 offset:96
	v_pk_fma_f32 v[20:21], v[20:21], v[176:177], v[84:85]
	v_pk_fma_f32 v[36:37], v[36:37], v[176:177], v[132:133]
	v_pk_fma_f32 v[54:55], v[54:55], v[178:179], v[156:157]
	v_pk_fma_f32 v[52:53], v[52:53], v[176:177], v[154:155]
	v_pk_fma_f32 v[26:27], v[26:27], v[182:183], v[90:91]
	v_pk_fma_f32 v[24:25], v[24:25], v[180:181], v[88:89]
	v_pk_fma_f32 v[42:43], v[42:43], v[182:183], v[144:145]
	v_pk_fma_f32 v[40:41], v[40:41], v[180:181], v[142:143]
	v_pk_fma_f32 v[58:59], v[58:59], v[182:183], v[160:161]
	v_pk_fma_f32 v[56:57], v[56:57], v[180:181], v[158:159]
	s_waitcnt lgkmcnt(0)
	v_pk_fma_f32 v[16:17], v[16:17], v[68:69], v[80:81]
	v_pk_fma_f32 v[18:19], v[18:19], v[70:71], v[82:83]
	v_pk_fma_f32 v[34:35], v[34:35], v[70:71], v[98:99]
	v_pk_fma_f32 v[32:33], v[32:33], v[68:69], v[96:97]
	v_pk_fma_f32 v[50:51], v[50:51], v[70:71], v[152:153]
	v_pk_fma_f32 v[48:49], v[48:49], v[68:69], v[150:151]
	v_pk_fma_f32 v[66:67], v[66:67], v[70:71], v[174:175]
	v_pk_fma_f32 v[64:65], v[64:65], v[68:69], v[172:173]
	global_store_dwordx4 v[162:163], v[4:7], off
	global_store_dwordx4 v[162:163], v[8:11], off offset:1024
	global_store_dwordx4 v[162:163], v[12:15], off offset:2048
	global_store_dwordx4 v[162:163], v[16:19], off offset:3072
	global_store_dwordx4 v[204:205], v[20:23], off
	global_store_dwordx4 v[204:205], v[24:27], off offset:1024
	global_store_dwordx4 v[204:205], v[28:31], off offset:2048
	global_store_dwordx4 v[204:205], v[32:35], off offset:3072
	global_store_dwordx4 v[208:209], v[36:39], off offset:-4096
	global_store_dwordx4 v[206:207], v[40:43], off offset:1024
	global_store_dwordx4 v[206:207], v[44:47], off offset:2048
	global_store_dwordx4 v[206:207], v[48:51], off offset:3072
	global_store_dwordx4 v[208:209], v[52:55], off
	global_store_dwordx4 v[208:209], v[56:59], off offset:1024
	global_store_dwordx4 v[208:209], v[60:63], off offset:2048
	global_store_dwordx4 v[208:209], v[64:67], off offset:3072
	v_mov_b32_e32 v19, 0
	v_mov_b32_e32 v18, 0
	v_mov_b32_e32 v17, 0
	v_mov_b32_e32 v16, 0
	v_mov_b32_e32 v15, 0
	v_mov_b32_e32 v14, 0
	v_mov_b32_e32 v13, 0
	v_mov_b32_e32 v12, 0
	v_mov_b32_e32 v11, 0
	v_mov_b32_e32 v10, 0
	v_mov_b32_e32 v9, 0
	v_mov_b32_e32 v8, 0
	v_mov_b32_e32 v7, 0
	v_mov_b32_e32 v6, 0
	v_mov_b32_e32 v5, 0
	v_mov_b32_e32 v4, 0
	v_mov_b32_e32 v67, 0
	v_mov_b32_e32 v66, 0
	v_mov_b32_e32 v65, 0
	v_mov_b32_e32 v64, 0
	v_mov_b32_e32 v63, 0
	v_mov_b32_e32 v62, 0
	v_mov_b32_e32 v61, 0
	v_mov_b32_e32 v60, 0
	v_mov_b32_e32 v59, 0
	v_mov_b32_e32 v58, 0
	v_mov_b32_e32 v57, 0
	v_mov_b32_e32 v56, 0
	v_mov_b32_e32 v55, 0
	v_mov_b32_e32 v54, 0
	v_mov_b32_e32 v53, 0
	v_mov_b32_e32 v52, 0
	v_mov_b32_e32 v51, 0
	v_mov_b32_e32 v50, 0
	v_mov_b32_e32 v49, 0
	v_mov_b32_e32 v48, 0
	v_mov_b32_e32 v47, 0
	v_mov_b32_e32 v46, 0
	v_mov_b32_e32 v45, 0
	v_mov_b32_e32 v44, 0
	v_mov_b32_e32 v43, 0
	v_mov_b32_e32 v42, 0
	v_mov_b32_e32 v41, 0
	v_mov_b32_e32 v40, 0
	v_mov_b32_e32 v39, 0
	v_mov_b32_e32 v38, 0
	v_mov_b32_e32 v37, 0
	v_mov_b32_e32 v36, 0
	v_mov_b32_e32 v35, 0
	v_mov_b32_e32 v34, 0
	v_mov_b32_e32 v33, 0
	v_mov_b32_e32 v32, 0
	v_mov_b32_e32 v31, 0
	v_mov_b32_e32 v30, 0
	v_mov_b32_e32 v29, 0
	v_mov_b32_e32 v28, 0
	v_mov_b32_e32 v27, 0
	v_mov_b32_e32 v26, 0
	v_mov_b32_e32 v25, 0
	v_mov_b32_e32 v24, 0
	v_mov_b32_e32 v23, 0
	v_mov_b32_e32 v22, 0
	v_mov_b32_e32 v21, 0
	v_mov_b32_e32 v20, 0
	s_cbranch_scc1 .LBB0_805
	s_lshl_b32 s2, s22, 1
	s_add_u32 s6, s6, s2
	s_addc_u32 s7, s7, 0
	s_add_u32 s2, s6, 0x1000
	s_addc_u32 s3, s7, 0
	s_add_u32 s6, s6, 0x1200
	s_addc_u32 s7, s7, 0
	s_add_i32 s17, 0, 0x21420
	v_mov_b32_e32 v2, s17
	s_waitcnt lgkmcnt(0)
	s_barrier
	ds_read_b32 v12, v2
	v_and_b32_e32 v2, 4, v203
	v_or3_b32 v158, v2, v202, v194
	v_mov_b64_e32 v[4:5], s[6:7]
	v_lshlrev_b32_e32 v10, 4, v139
	s_waitcnt lgkmcnt(0)
	v_add_u32_e32 v13, v12, v189
	v_add_u32_e32 v2, v13, v158
	v_mad_i64_i32 v[6:7], s[10:11], v2, s76, v[4:5]
	s_lshl_b32 s10, s68, 10
	v_lshlrev_b32_e32 v2, 1, v201
	s_add_i32 s46, s10, 0
	v_lshl_add_u64 v[6:7], v[6:7], 0, v[2:3]
	s_mov_b32 m0, s46
	v_add_u32_e32 v8, v12, v188
	global_load_lds_dwordx4 v[6:7], off
	v_mov_b64_e32 v[6:7], s[2:3]
	v_mad_i64_i32 v[8:9], s[10:11], v8, s76, v[6:7]
	v_mov_b32_e32 v11, v3
	v_ashrrev_i32_e32 v159, 8, v195
	v_lshl_add_u64 v[8:9], v[8:9], 0, v[10:11]
	s_add_i32 m0, s46, 0x4000
	v_lshrrev_b32_e32 v10, 1, v159
	global_load_lds_dwordx4 v[8:9], off
	v_and_b32_e32 v9, -16, v159
	v_and_b32_e32 v10, 4, v10
	v_or3_b32 v160, v9, v10, v194
	v_add_u32_e32 v9, v13, v160
	v_mad_i64_i32 v[4:5], s[10:11], v9, s76, v[4:5]
	v_lshl_add_u64 v[4:5], v[4:5], 0, v[2:3]
	s_add_i32 m0, s46, 0x2000
	v_bitop3_b32 v8, v159, v193, 7 bitop3:0x6c
	global_load_lds_dwordx4 v[4:5], off
	v_add_u32_e32 v4, v12, v159
	v_mad_i64_i32 v[4:5], s[10:11], v4, s76, v[6:7]
	v_lshlrev_b32_e32 v6, 4, v8
	v_mov_b32_e32 v7, v3
	v_lshl_add_u64 v[4:5], v[4:5], 0, v[6:7]
	s_add_i32 m0, s46, 0x6000
	v_readlane_b32 s10, v255, 24
	global_load_lds_dwordx4 v[4:5], off
	v_lshlrev_b32_e32 v4, 3, v139
	v_lshlrev_b32_e32 v5, 3, v8
	s_cmp_eq_u32 s65, s10
	v_lshlrev_b32_e32 v6, 1, v4
	v_lshlrev_b32_e32 v4, 1, v5
	s_cbranch_scc1 .LBB0_785
	v_readlane_b32 s10, v255, 19
	v_mov_b64_e32 v[8:9], s[6:7]
	s_add_i32 m0, s46, 0x8000
	v_mov_b32_e32 v5, s10
	ds_read_b32 v5, v5
	s_waitcnt lgkmcnt(0)
	v_add_u32_e32 v14, v5, v189
	v_add_u32_e32 v7, v14, v158
	v_mad_i64_i32 v[10:11], s[10:11], v7, s76, v[8:9]
	v_lshl_add_u64 v[10:11], v[10:11], 0, v[2:3]
	global_load_lds_dwordx4 v[10:11], off
	v_add_u32_e32 v7, v5, v188
	v_mov_b64_e32 v[10:11], s[2:3]
	v_mad_i64_i32 v[12:13], s[10:11], v7, s76, v[10:11]
	v_mov_b32_e32 v7, v3
	v_lshl_add_u64 v[12:13], v[12:13], 0, v[6:7]
	v_add_u32_e32 v7, v14, v160
	s_add_i32 m0, s46, 0xc000
	v_mad_i64_i32 v[8:9], s[10:11], v7, s76, v[8:9]
	global_load_lds_dwordx4 v[12:13], off
	v_lshl_add_u64 v[8:9], v[8:9], 0, v[2:3]
	s_add_i32 m0, s46, 0xa000
	v_add_u32_e32 v5, v5, v159
	global_load_lds_dwordx4 v[8:9], off
	v_mad_i64_i32 v[8:9], s[10:11], v5, s76, v[10:11]
	v_mov_b32_e32 v5, v3
	v_lshl_add_u64 v[8:9], v[8:9], 0, v[4:5]
	s_add_i32 m0, s46, 0xe000
	s_nop 0
	global_load_lds_dwordx4 v[8:9], off

.LBB0_1169:
	s_or_b64 exec, exec, s[0:1]
	v_ashrrev_i32_e32 v196, 4, v34
	v_and_b32_e32 v1, 15, v34
	v_lshlrev_b32_e32 v8, 2, v196
	v_lshlrev_b32_e32 v194, 3, v1
	v_mov_b32_e32 v195, 0
	v_ashrrev_i32_e32 v9, 31, v8
	v_lshl_add_u64 v[6:7], s[82:83], 0, v[194:195]
	v_lshlrev_b64 v[2:3], 7, v[8:9]
	v_lshl_add_u64 v[10:11], v[6:7], 0, v[2:3]
	v_or_b32_e32 v2, 2, v8
	v_ashrrev_i32_e32 v3, 31, v2
	v_lshlrev_b64 v[2:3], 7, v[2:3]
	v_lshl_add_u64 v[12:13], v[6:7], 0, v[2:3]
	global_load_dwordx2 v[4:5], v[10:11], off
	global_load_dwordx2 v[36:37], v[10:11], off offset:128
	global_load_dwordx2 v[2:3], v[12:13], off
	global_load_dwordx2 v[38:39], v[12:13], off offset:128
	v_or_b32_e32 v10, 0x80, v8
	v_ashrrev_i32_e32 v11, 31, v10
	v_lshlrev_b64 v[10:11], 7, v[10:11]
	v_lshl_add_u64 v[14:15], v[6:7], 0, v[10:11]
	v_or_b32_e32 v10, 0x82, v8
	v_ashrrev_i32_e32 v11, 31, v10
	v_lshlrev_b64 v[10:11], 7, v[10:11]
	v_lshl_add_u64 v[16:17], v[6:7], 0, v[10:11]
	global_load_dwordx2 v[12:13], v[14:15], off
	global_load_dwordx2 v[40:41], v[14:15], off offset:128
	global_load_dwordx2 v[10:11], v[16:17], off
	global_load_dwordx2 v[42:43], v[16:17], off offset:128
	v_or_b32_e32 v14, 0x100, v8
	v_ashrrev_i32_e32 v15, 31, v14
	v_lshlrev_b64 v[14:15], 7, v[14:15]
	v_lshl_add_u64 v[18:19], v[6:7], 0, v[14:15]
	v_or_b32_e32 v14, 0x102, v8
	v_ashrrev_i32_e32 v15, 31, v14
	v_lshlrev_b64 v[14:15], 7, v[14:15]
	v_lshl_add_u64 v[20:21], v[6:7], 0, v[14:15]
	global_load_dwordx2 v[16:17], v[18:19], off
	global_load_dwordx2 v[44:45], v[18:19], off offset:128
	global_load_dwordx2 v[14:15], v[20:21], off
	global_load_dwordx2 v[46:47], v[20:21], off offset:128
	v_or_b32_e32 v18, 0x180, v8
	v_ashrrev_i32_e32 v19, 31, v18
	v_lshlrev_b64 v[18:19], 7, v[18:19]
	v_lshl_add_u64 v[22:23], v[6:7], 0, v[18:19]
	v_or_b32_e32 v18, 0x182, v8
	v_ashrrev_i32_e32 v19, 31, v18
	v_lshlrev_b64 v[18:19], 7, v[18:19]
	v_lshl_add_u64 v[24:25], v[6:7], 0, v[18:19]
	global_load_dwordx2 v[20:21], v[22:23], off
	global_load_dwordx2 v[48:49], v[22:23], off offset:128
	global_load_dwordx2 v[18:19], v[24:25], off
	global_load_dwordx2 v[50:51], v[24:25], off offset:128
	v_or_b32_e32 v22, 0x200, v8
	v_ashrrev_i32_e32 v23, 31, v22
	v_lshlrev_b64 v[22:23], 7, v[22:23]
	v_lshl_add_u64 v[26:27], v[6:7], 0, v[22:23]
	v_or_b32_e32 v22, 0x202, v8
	v_ashrrev_i32_e32 v23, 31, v22
	v_lshlrev_b64 v[22:23], 7, v[22:23]
	v_lshl_add_u64 v[28:29], v[6:7], 0, v[22:23]
	global_load_dwordx2 v[24:25], v[26:27], off
	global_load_dwordx2 v[52:53], v[26:27], off offset:128
	global_load_dwordx2 v[22:23], v[28:29], off
	global_load_dwordx2 v[54:55], v[28:29], off offset:128
	v_or_b32_e32 v26, 0x280, v8
	v_ashrrev_i32_e32 v27, 31, v26
	v_lshlrev_b64 v[26:27], 7, v[26:27]
	v_lshl_add_u64 v[30:31], v[6:7], 0, v[26:27]
	v_or_b32_e32 v26, 0x282, v8
	v_ashrrev_i32_e32 v27, 31, v26
	v_lshlrev_b64 v[26:27], 7, v[26:27]
	v_lshl_add_u64 v[32:33], v[6:7], 0, v[26:27]
	global_load_dwordx2 v[28:29], v[30:31], off
	global_load_dwordx2 v[56:57], v[30:31], off offset:128
	global_load_dwordx2 v[26:27], v[32:33], off
	global_load_dwordx2 v[58:59], v[32:33], off offset:128
	v_or_b32_e32 v30, 0x300, v8
	v_ashrrev_i32_e32 v31, 31, v30
	v_lshlrev_b64 v[30:31], 7, v[30:31]
	v_lshl_add_u64 v[64:65], v[6:7], 0, v[30:31]
	v_or_b32_e32 v30, 0x302, v8
	v_ashrrev_i32_e32 v31, 31, v30
	v_lshlrev_b64 v[30:31], 7, v[30:31]
	v_lshl_add_u64 v[66:67], v[6:7], 0, v[30:31]
	global_load_dwordx2 v[32:33], v[64:65], off
	global_load_dwordx2 v[60:61], v[64:65], off offset:128
	global_load_dwordx2 v[30:31], v[66:67], off
	global_load_dwordx2 v[62:63], v[66:67], off offset:128
	v_or_b32_e32 v64, 0x380, v8
	v_ashrrev_i32_e32 v65, 31, v64
	v_lshlrev_b64 v[64:65], 7, v[64:65]
	v_lshl_add_u64 v[68:69], v[6:7], 0, v[64:65]
	v_or_b32_e32 v64, 0x382, v8
	v_ashrrev_i32_e32 v65, 31, v64
	v_lshlrev_b64 v[64:65], 7, v[64:65]
	v_lshl_add_u64 v[70:71], v[6:7], 0, v[64:65]
	global_load_dwordx2 v[130:131], v[68:69], off
	global_load_dwordx2 v[64:65], v[68:69], off offset:128
	global_load_dwordx2 v[132:133], v[70:71], off
	global_load_dwordx2 v[66:67], v[70:71], off offset:128
	v_or_b32_e32 v68, 0x400, v8
	v_ashrrev_i32_e32 v69, 31, v68
	v_lshlrev_b64 v[68:69], 7, v[68:69]
	v_lshl_add_u64 v[72:73], v[6:7], 0, v[68:69]
	v_or_b32_e32 v68, 0x402, v8
	v_ashrrev_i32_e32 v69, 31, v68
	v_lshlrev_b64 v[68:69], 7, v[68:69]
	v_lshl_add_u64 v[74:75], v[6:7], 0, v[68:69]
	global_load_dwordx2 v[134:135], v[72:73], off
	global_load_dwordx2 v[68:69], v[72:73], off offset:128
	global_load_dwordx2 v[136:137], v[74:75], off
	global_load_dwordx2 v[70:71], v[74:75], off offset:128
	v_or_b32_e32 v72, 0x480, v8
	v_ashrrev_i32_e32 v73, 31, v72
	v_lshlrev_b64 v[72:73], 7, v[72:73]
	v_lshl_add_u64 v[76:77], v[6:7], 0, v[72:73]
	v_or_b32_e32 v72, 0x482, v8
	v_ashrrev_i32_e32 v73, 31, v72
	v_lshlrev_b64 v[72:73], 7, v[72:73]
	v_lshl_add_u64 v[78:79], v[6:7], 0, v[72:73]
	global_load_dwordx2 v[138:139], v[76:77], off
	global_load_dwordx2 v[72:73], v[76:77], off offset:128
	global_load_dwordx2 v[140:141], v[78:79], off
	global_load_dwordx2 v[74:75], v[78:79], off offset:128
	v_or_b32_e32 v76, 0x500, v8
	v_ashrrev_i32_e32 v77, 31, v76
	v_lshlrev_b64 v[76:77], 7, v[76:77]
	v_lshl_add_u64 v[80:81], v[6:7], 0, v[76:77]
	v_or_b32_e32 v76, 0x502, v8
	v_ashrrev_i32_e32 v77, 31, v76
	v_lshlrev_b64 v[76:77], 7, v[76:77]
	v_lshl_add_u64 v[82:83], v[6:7], 0, v[76:77]
	global_load_dwordx2 v[142:143], v[80:81], off
	global_load_dwordx2 v[76:77], v[80:81], off offset:128
	global_load_dwordx2 v[144:145], v[82:83], off
	global_load_dwordx2 v[78:79], v[82:83], off offset:128
	v_or_b32_e32 v80, 0x580, v8
	v_ashrrev_i32_e32 v81, 31, v80
	v_lshlrev_b64 v[80:81], 7, v[80:81]
	v_lshl_add_u64 v[84:85], v[6:7], 0, v[80:81]
	v_or_b32_e32 v80, 0x582, v8
	v_ashrrev_i32_e32 v81, 31, v80
	v_lshlrev_b64 v[80:81], 7, v[80:81]
	v_lshl_add_u64 v[86:87], v[6:7], 0, v[80:81]
	global_load_dwordx2 v[146:147], v[84:85], off
	global_load_dwordx2 v[80:81], v[84:85], off offset:128
	global_load_dwordx2 v[150:151], v[86:87], off
	global_load_dwordx2 v[82:83], v[86:87], off offset:128
	v_or_b32_e32 v84, 0x600, v8
	v_ashrrev_i32_e32 v85, 31, v84
	v_lshlrev_b64 v[84:85], 7, v[84:85]
	v_lshl_add_u64 v[88:89], v[6:7], 0, v[84:85]
	v_or_b32_e32 v84, 0x602, v8
	v_ashrrev_i32_e32 v85, 31, v84
	v_lshlrev_b64 v[84:85], 7, v[84:85]
	v_lshl_add_u64 v[90:91], v[6:7], 0, v[84:85]
	global_load_dwordx2 v[154:155], v[88:89], off
	global_load_dwordx2 v[84:85], v[88:89], off offset:128
	global_load_dwordx2 v[160:161], v[90:91], off
	global_load_dwordx2 v[86:87], v[90:91], off offset:128
	v_or_b32_e32 v88, 0x680, v8
	v_ashrrev_i32_e32 v89, 31, v88
	v_lshlrev_b64 v[88:89], 7, v[88:89]
	v_lshl_add_u64 v[92:93], v[6:7], 0, v[88:89]
	v_or_b32_e32 v88, 0x682, v8
	v_ashrrev_i32_e32 v89, 31, v88
	v_lshlrev_b64 v[88:89], 7, v[88:89]
	v_lshl_add_u64 v[94:95], v[6:7], 0, v[88:89]
	global_load_dwordx2 v[162:163], v[92:93], off
	global_load_dwordx2 v[88:89], v[92:93], off offset:128
	global_load_dwordx2 v[164:165], v[94:95], off
	global_load_dwordx2 v[90:91], v[94:95], off offset:128
	v_or_b32_e32 v92, 0x700, v8
	v_ashrrev_i32_e32 v93, 31, v92
	v_lshlrev_b64 v[92:93], 7, v[92:93]
	v_lshl_add_u64 v[94:95], v[6:7], 0, v[92:93]
	v_or_b32_e32 v92, 0x702, v8
	v_ashrrev_i32_e32 v93, 31, v92
	v_lshlrev_b64 v[92:93], 7, v[92:93]
	v_lshl_add_u64 v[96:97], v[6:7], 0, v[92:93]
	global_load_dwordx2 v[168:169], v[94:95], off
	global_load_dwordx2 v[92:93], v[94:95], off offset:128
	global_load_dwordx2 v[170:171], v[96:97], off
	s_nop 0
	global_load_dwordx2 v[94:95], v[96:97], off offset:128
	v_or_b32_e32 v96, 0x780, v8
	v_ashrrev_i32_e32 v97, 31, v96
	v_or_b32_e32 v8, 0x782, v8
	v_lshlrev_b64 v[96:97], 7, v[96:97]
	v_ashrrev_i32_e32 v9, 31, v8
	v_lshl_add_u64 v[96:97], v[6:7], 0, v[96:97]
	v_lshlrev_b64 v[8:9], 7, v[8:9]
	v_lshl_add_u64 v[6:7], v[6:7], 0, v[8:9]
	global_load_dwordx2 v[172:173], v[96:97], off
	s_nop 0
	global_load_dwordx2 v[96:97], v[96:97], off offset:128
	s_nop 0
	global_load_dwordx2 v[180:181], v[6:7], off
	global_load_dwordx2 v[98:99], v[6:7], off offset:128
	s_cmpk_gt_i32 s72, 0xfff
	s_waitcnt lgkmcnt(0)
	s_barrier
	s_cbranch_scc1 .LBB0_1183
	v_ashrrev_i32_e32 v1, 6, v34
	s_add_u32 s0, s96, 0x5dd70000
	v_and_b32_e32 v35, 63, v34
	s_addc_u32 s1, s97, 0
	v_lshlrev_b32_e32 v182, 13, v1
	s_waitcnt vmcnt(61)
	v_mov_b32_e32 v102, v2
	s_add_u32 s2, s96, 0x5dd71000
	v_lshl_add_u32 v2, s72, 16, v182
	v_lshlrev_b32_e32 v199, 4, v35
	v_lshlrev_b32_e32 v212, 3, v35
	v_readlane_b32 s8, v254, 11
	s_waitcnt vmcnt(37)
	v_mov_b32_e32 v126, v30
	s_waitcnt vmcnt(35)
	v_mov_b32_e32 v128, v130
	s_waitcnt vmcnt(33)
	v_mov_b32_e32 v130, v132
	s_waitcnt vmcnt(31)
	v_mov_b32_e32 v132, v134
	s_waitcnt vmcnt(29)
	v_mov_b32_e32 v134, v136
	s_waitcnt vmcnt(27)
	v_mov_b32_e32 v136, v138
	s_waitcnt vmcnt(25)
	v_mov_b32_e32 v138, v140
	s_addc_u32 s3, s97, 0
	v_or_b32_e32 v30, v2, v199
	v_or_b32_e32 v140, v2, v212
	v_readlane_b32 s9, v254, 12
	v_mov_b32_e32 v100, v4
	v_mov_b32_e32 v101, v36
	v_mov_b32_e32 v36, v5
	v_mov_b32_e32 v103, v38
	v_mov_b32_e32 v38, v3
	v_mov_b32_e32 v104, v12
	v_mov_b32_e32 v105, v40
	v_mov_b32_e32 v40, v13
	v_mov_b32_e32 v106, v10
	v_mov_b32_e32 v107, v42
	v_mov_b32_e32 v42, v11
	v_mov_b32_e32 v108, v16
	v_mov_b32_e32 v109, v44
	v_mov_b32_e32 v44, v17
	v_mov_b32_e32 v110, v14
	v_mov_b32_e32 v111, v46
	v_mov_b32_e32 v46, v15
	v_mov_b32_e32 v112, v20
	v_mov_b32_e32 v114, v18
	v_mov_b32_e32 v115, v50
	v_mov_b32_e32 v50, v19
	v_mov_b32_e32 v118, v22
	v_mov_b32_e32 v122, v26
	v_mov_b32_e32 v127, v62
	v_mov_b32_e32 v62, v31
	global_load_dwordx4 v[2:5], v30, s[8:9]
	global_load_dwordx4 v[6:9], v30, s[8:9] offset:1024
	v_or_b32_e32 v18, 0x200, v140
	v_or_b32_e32 v19, 0x400, v140
	global_load_dwordx4 v[10:13], v30, s[8:9] offset:2048
	global_load_dwordx4 v[14:17], v30, s[8:9] offset:3072
	v_or_b32_e32 v20, 0x600, v140
	global_load_dwordx2 v[148:149], v140, s[2:3]
	global_load_dwordx2 v[152:153], v18, s[2:3]
	global_load_dwordx2 v[156:157], v19, s[2:3]
	global_load_dwordx2 v[158:159], v20, s[2:3]
	v_or_b32_e32 v22, 0x800, v140
	v_or_b32_e32 v26, 0xa00, v140
	v_or_b32_e32 v31, 0xc00, v140
	v_or_b32_e32 v140, 0xe00, v140
	v_or_b32_e32 v18, 0x1000, v30
	global_load_dwordx2 v[166:167], v22, s[2:3]
	global_load_dwordx2 v[174:175], v26, s[2:3]
	global_load_dwordx2 v[176:177], v31, s[2:3]
	global_load_dwordx2 v[178:179], v140, s[2:3]
	v_or_b32_e32 v22, 0x1400, v30
	v_or_b32_e32 v26, 0x1800, v30
	v_or_b32_e32 v30, 0x1c00, v30
	v_mov_b32_e32 v113, v48
	v_mov_b32_e32 v48, v21
	v_mov_b32_e32 v116, v24
	v_mov_b32_e32 v117, v52
	v_mov_b32_e32 v52, v25
	v_mov_b32_e32 v119, v54
	v_mov_b32_e32 v54, v23
	v_mov_b32_e32 v120, v28
	v_mov_b32_e32 v121, v56
	v_mov_b32_e32 v56, v29
	v_mov_b32_e32 v123, v58
	v_mov_b32_e32 v58, v27
	v_mov_b32_e32 v124, v32
	v_mov_b32_e32 v125, v60
	v_mov_b32_e32 v60, v33
	global_load_dwordx4 v[18:21], v18, s[8:9]
	s_add_u32 s4, s96, 0x32370000
	global_load_dwordx4 v[22:25], v22, s[8:9]
	v_readlane_b32 s14, v254, 17
	global_load_dwordx4 v[26:29], v26, s[8:9]
	s_addc_u32 s5, s97, 0
	global_load_dwordx4 v[30:33], v30, s[8:9]
	v_readlane_b32 s15, v254, 18
	s_add_u32 s14, s96, 0x6dd70000
	v_lshlrev_b32_e32 v215, 2, v35
	v_ashrrev_i32_e32 v35, 31, v34
	v_readlane_b32 s10, v254, 13
	v_readlane_b32 s11, v254, 14
	v_readlane_b32 s16, v254, 19
	s_addc_u32 s15, s97, 0
	v_lshlrev_b64 v[192:193], 2, v[34:35]
	v_mov_b32_e32 v129, v64
	v_mov_b32_e32 v64, v131
	v_mov_b32_e32 v131, v66
	v_mov_b32_e32 v66, v133
	v_mov_b32_e32 v133, v68
	v_mov_b32_e32 v68, v135
	v_mov_b32_e32 v135, v70
	v_mov_b32_e32 v70, v137
	v_mov_b32_e32 v137, v72
	v_mov_b32_e32 v72, v139
	s_waitcnt vmcnt(40)
	v_mov_b32_e32 v139, v74
	v_mov_b32_e32 v74, v141
	v_readlane_b32 s17, v254, 20
	s_waitcnt vmcnt(39)
	v_mov_b32_e32 v140, v142
	s_waitcnt vmcnt(38)
	v_mov_b32_e32 v141, v76
	v_mov_b32_e32 v76, v143
	s_waitcnt vmcnt(37)
	v_mov_b32_e32 v142, v144
	s_waitcnt vmcnt(36)
	v_mov_b32_e32 v143, v78
	v_mov_b32_e32 v78, v145
	s_waitcnt vmcnt(35)
	v_mov_b32_e32 v144, v146
	s_waitcnt vmcnt(34)
	v_mov_b32_e32 v145, v80
	v_mov_b32_e32 v80, v147
	s_waitcnt vmcnt(33)
	v_mov_b32_e32 v146, v150
	s_waitcnt vmcnt(32)
	v_mov_b32_e32 v147, v82
	v_mov_b32_e32 v82, v151
	s_waitcnt vmcnt(31)
	v_mov_b32_e32 v150, v154
	s_waitcnt vmcnt(30)
	v_mov_b32_e32 v151, v84
	v_mov_b32_e32 v84, v155
	s_waitcnt vmcnt(29)
	v_mov_b32_e32 v154, v160
	s_waitcnt vmcnt(28)
	v_mov_b32_e32 v155, v86
	v_mov_b32_e32 v86, v161
	s_waitcnt vmcnt(27)
	v_mov_b32_e32 v160, v162
	s_waitcnt vmcnt(26)
	v_mov_b32_e32 v161, v88
	v_mov_b32_e32 v88, v163
	s_waitcnt vmcnt(25)
	v_mov_b32_e32 v162, v164
	s_waitcnt vmcnt(24)
	v_mov_b32_e32 v163, v90
	v_mov_b32_e32 v90, v165
	s_waitcnt vmcnt(23)
	v_mov_b32_e32 v164, v168
	s_waitcnt vmcnt(22)
	v_mov_b32_e32 v165, v92
	v_mov_b32_e32 v92, v169
	s_waitcnt vmcnt(21)
	v_mov_b32_e32 v168, v170
	s_waitcnt vmcnt(20)
	v_mov_b32_e32 v169, v94
	v_mov_b32_e32 v94, v171
	s_waitcnt vmcnt(19)
	v_mov_b32_e32 v170, v172
	s_waitcnt vmcnt(18)
	v_mov_b32_e32 v171, v96
	v_mov_b32_e32 v96, v173
	s_waitcnt vmcnt(17)
	v_mov_b32_e32 v172, v180
	s_waitcnt vmcnt(16)
	v_mov_b32_e32 v173, v98
	v_mov_b32_e32 v98, v181
	s_add_u32 s16, s96, 0x6ddf0000
	v_add3_u32 v216, 0, v182, v199
	v_lshl_add_u64 v[180:181], s[78:79], 0, v[192:193]
	v_lshl_add_u64 v[182:183], s[80:81], 0, v[192:193]
	s_mov_b64 s[10:11], 0x1000
	v_readlane_b32 s18, v254, 21
	s_addc_u32 s17, s97, 0
	s_add_i32 s8, 0, 0x19000
	v_lshl_add_u64 v[184:185], v[180:181], 0, s[10:11]
	v_lshl_add_u64 v[186:187], v[182:183], 0, s[10:11]
	s_mov_b64 s[10:11], 0x1800
	v_lshl_or_b32 v35, v196, 7, v194
	v_readlane_b32 s19, v254, 22
	v_readlane_b32 s20, v254, 23
	v_readlane_b32 s21, v254, 24
	v_lshl_add_u32 v213, v34, 2, s8
	v_add_u32_e32 v214, s8, v199
	s_add_u32 s18, s74, 0xf8
	s_movk_i32 s8, 0x100
	v_lshl_add_u64 v[188:189], v[180:181], 0, s[10:11]
	v_lshl_add_u64 v[190:191], v[182:183], 0, s[10:11]
	v_lshl_add_u64 v[192:193], s[96:97], 0, v[192:193]
	s_mov_b64 s[10:11], 0x10000
	v_add_u32_e32 v35, 0, v35
	s_addc_u32 s19, s75, 0
	v_cmp_gt_i32_e64 s[8:9], s8, v34
	v_lshl_add_u64 v[192:193], v[192:193], 0, s[10:11]
	v_add_u32_e32 v35, 0x10000, v35
	v_lshl_add_u32 v217, v196, 4, 0
	s_mov_b32 s29, -1
	s_mov_b32 s20, 0x3f9837f0
	v_mov_b32_e32 v218, 0x3727c5ac
	s_mov_b32 s21, 0x800000
	s_add_i32 s26, 0, 0x18000
	s_add_i32 s27, 0, 0x18480
	v_mov_b32_e32 v219, 1
	s_mov_b32 s28, s72
	v_readlane_b32 s12, v254, 15
	v_readlane_b32 s13, v254, 16
	v_readlane_b32 s22, v254, 25
	v_readlane_b32 s23, v254, 26
	s_branch .LBB0_1172

.LBB0_1176:
	s_mov_b32 s10, 0
	v_mov_b32_e32 v194, v217
	s_barrier
	ds_read_b128 v[200:203], v194
	ds_read_b128 v[204:207], v194 offset:512
	ds_read_b128 v[208:211], v194 offset:1024
	ds_read_b128 v[228:231], v194 offset:1536
	ds_read_b128 v[232:235], v194 offset:2048
	ds_read_b128 v[236:239], v194 offset:2560
	ds_read_b128 v[240:243], v194 offset:3072
	ds_read_b128 v[244:247], v194 offset:3584
	ds_write_b64 v35, v[248:249]
.LBB0_1177:
	s_waitcnt lgkmcnt(8)
	v_pk_fma_f32 v[196:197], v[200:201], v[100:101], 0 op_sel_hi:[1,1,0]
	v_pk_fma_f32 v[222:223], v[202:203], v[102:103], 0 op_sel_hi:[1,1,0]
	v_pk_fma_f32 v[224:225], v[200:201], v[36:37], 0 op_sel_hi:[1,1,0]
	v_pk_fma_f32 v[226:227], v[202:203], v[38:39], 0 op_sel_hi:[1,1,0]
	ds_read_b128 v[200:203], v194 offset:4096
	s_waitcnt lgkmcnt(8)
	v_pk_fma_f32 v[196:197], v[204:205], v[104:105], v[196:197]
	v_pk_fma_f32 v[222:223], v[206:207], v[106:107], v[222:223]
	v_pk_fma_f32 v[224:225], v[204:205], v[40:41], v[224:225]
	v_pk_fma_f32 v[226:227], v[206:207], v[42:43], v[226:227]
	ds_read_b128 v[204:207], v194 offset:4608
	s_waitcnt lgkmcnt(8)
	v_pk_fma_f32 v[196:197], v[208:209], v[108:109], v[196:197]
	v_pk_fma_f32 v[222:223], v[210:211], v[110:111], v[222:223]
	v_pk_fma_f32 v[224:225], v[208:209], v[44:45], v[224:225]
	v_pk_fma_f32 v[226:227], v[210:211], v[46:47], v[226:227]
	ds_read_b128 v[208:211], v194 offset:5120
	s_waitcnt lgkmcnt(8)
	v_pk_fma_f32 v[196:197], v[228:229], v[112:113], v[196:197]
	v_pk_fma_f32 v[222:223], v[230:231], v[114:115], v[222:223]
	v_pk_fma_f32 v[224:225], v[228:229], v[48:49], v[224:225]
	v_pk_fma_f32 v[226:227], v[230:231], v[50:51], v[226:227]
	ds_read_b128 v[228:231], v194 offset:5632
	s_waitcnt lgkmcnt(8)
	v_pk_fma_f32 v[196:197], v[232:233], v[116:117], v[196:197]
	v_pk_fma_f32 v[222:223], v[234:235], v[118:119], v[222:223]
	v_pk_fma_f32 v[224:225], v[232:233], v[52:53], v[224:225]
	v_pk_fma_f32 v[226:227], v[234:235], v[54:55], v[226:227]
	ds_read_b128 v[232:235], v194 offset:6144
	s_waitcnt lgkmcnt(8)
	v_pk_fma_f32 v[196:197], v[236:237], v[120:121], v[196:197]
	v_pk_fma_f32 v[222:223], v[238:239], v[122:123], v[222:223]
	v_pk_fma_f32 v[224:225], v[236:237], v[56:57], v[224:225]
	v_pk_fma_f32 v[226:227], v[238:239], v[58:59], v[226:227]
	ds_read_b128 v[236:239], v194 offset:6656
	s_waitcnt lgkmcnt(8)
	v_pk_fma_f32 v[196:197], v[240:241], v[124:125], v[196:197]
	v_pk_fma_f32 v[222:223], v[242:243], v[126:127], v[222:223]
	v_pk_fma_f32 v[224:225], v[240:241], v[60:61], v[224:225]
	v_pk_fma_f32 v[226:227], v[242:243], v[62:63], v[226:227]
	ds_read_b128 v[240:243], v194 offset:7168
	s_waitcnt lgkmcnt(8)
	v_pk_fma_f32 v[196:197], v[244:245], v[128:129], v[196:197]
	v_pk_fma_f32 v[222:223], v[246:247], v[130:131], v[222:223]
	v_pk_fma_f32 v[224:225], v[244:245], v[64:65], v[224:225]
	v_pk_fma_f32 v[226:227], v[246:247], v[66:67], v[226:227]
	ds_read_b128 v[244:247], v194 offset:7680
	s_waitcnt lgkmcnt(7)
	v_pk_fma_f32 v[196:197], v[200:201], v[132:133], v[196:197]
	v_pk_fma_f32 v[222:223], v[202:203], v[134:135], v[222:223]
	v_pk_fma_f32 v[224:225], v[200:201], v[68:69], v[224:225]
	v_pk_fma_f32 v[226:227], v[202:203], v[70:71], v[226:227]
	ds_read_b128 v[200:203], v194 offset:8192
	s_waitcnt lgkmcnt(7)
	v_pk_fma_f32 v[196:197], v[204:205], v[136:137], v[196:197]
	v_pk_fma_f32 v[222:223], v[206:207], v[138:139], v[222:223]
	v_pk_fma_f32 v[224:225], v[204:205], v[72:73], v[224:225]
	v_pk_fma_f32 v[226:227], v[206:207], v[74:75], v[226:227]
	ds_read_b128 v[204:207], v194 offset:8704
	s_waitcnt lgkmcnt(7)
	v_pk_fma_f32 v[196:197], v[208:209], v[140:141], v[196:197]
	v_pk_fma_f32 v[222:223], v[210:211], v[142:143], v[222:223]
	v_pk_fma_f32 v[224:225], v[208:209], v[76:77], v[224:225]
	v_pk_fma_f32 v[226:227], v[210:211], v[78:79], v[226:227]
	ds_read_b128 v[208:211], v194 offset:9216
	s_waitcnt lgkmcnt(7)
	v_pk_fma_f32 v[196:197], v[228:229], v[144:145], v[196:197]
	v_pk_fma_f32 v[222:223], v[230:231], v[146:147], v[222:223]
	v_pk_fma_f32 v[224:225], v[228:229], v[80:81], v[224:225]
	v_pk_fma_f32 v[226:227], v[230:231], v[82:83], v[226:227]
	ds_read_b128 v[228:231], v194 offset:9728
	s_waitcnt lgkmcnt(7)
	v_pk_fma_f32 v[196:197], v[232:233], v[150:151], v[196:197]
	v_pk_fma_f32 v[222:223], v[234:235], v[154:155], v[222:223]
	v_pk_fma_f32 v[224:225], v[232:233], v[84:85], v[224:225]
	v_pk_fma_f32 v[226:227], v[234:235], v[86:87], v[226:227]
	ds_read_b128 v[232:235], v194 offset:10240
	s_waitcnt lgkmcnt(7)
	v_pk_fma_f32 v[196:197], v[236:237], v[160:161], v[196:197]
	v_pk_fma_f32 v[222:223], v[238:239], v[162:163], v[222:223]
	v_pk_fma_f32 v[224:225], v[236:237], v[88:89], v[224:225]
	v_pk_fma_f32 v[226:227], v[238:239], v[90:91], v[226:227]
	ds_read_b128 v[236:239], v194 offset:10752
	s_waitcnt lgkmcnt(7)
	v_pk_fma_f32 v[196:197], v[240:241], v[164:165], v[196:197]
	v_pk_fma_f32 v[222:223], v[242:243], v[168:169], v[222:223]
	v_pk_fma_f32 v[224:225], v[240:241], v[92:93], v[224:225]
	v_pk_fma_f32 v[226:227], v[242:243], v[94:95], v[226:227]
	ds_read_b128 v[240:243], v194 offset:11264
	s_waitcnt lgkmcnt(7)
	v_pk_fma_f32 v[196:197], v[244:245], v[170:171], v[196:197]
	v_pk_fma_f32 v[222:223], v[246:247], v[172:173], v[222:223]
	v_pk_fma_f32 v[224:225], v[244:245], v[96:97], v[224:225]
	v_pk_fma_f32 v[226:227], v[246:247], v[98:99], v[226:227]
	ds_read_b128 v[244:247], v194 offset:11776
	v_add_u32_e32 v195, s10, v35
	s_addk_i32 s10, 0x1000
	v_add_u32_e32 v194, 0x2000, v194
	v_add_f32_e32 v248, v196, v197
	v_add_f32_e32 v249, v222, v223
	v_add_f32_e32 v250, v224, v225
	v_add_f32_e32 v251, v226, v227
	v_add_f32_e32 v248, v248, v249
	v_add_f32_e32 v249, v250, v251
	s_cmpk_eq_u32 s10, 0x8000
	ds_write_b64 v195, v[248:249]
	s_cbranch_scc0 .LBB0_1177
	s_waitcnt lgkmcnt(0)
	s_barrier
	s_and_saveexec_b64 s[24:25], s[8:9]
	s_cbranch_execz .LBB0_1171
	v_mov_b32_e32 v198, v0
	s_add_i32 s10, 0, 0x10000
	v_and_b32_e32 v194, 31, v198
	v_lshlrev_b32_e32 v195, 2, v194
	v_add_u32_e32 v196, s26, v195
	ds_read_b32 v202, v196 offset:1280
	v_lshlrev_b32_e32 v196, 7, v198
	v_and_b32_e32 v196, 0xfffff000, v196
	v_add3_u32 v195, s10, v195, v196
	ds_read2_b32 v[196:197], v195 offset1:32
	ds_read2_b32 v[200:201], v195 offset0:64 offset1:96
	v_add_u32_e32 v204, 0x400, v195
	v_cmp_ne_u32_e64 s[12:13], 0, v194
	s_waitcnt lgkmcnt(1)
	v_add_f32_e32 v196, v202, v196
	ds_read2_b32 v[202:203], v195 offset0:128 offset1:160
	v_add_f32_e32 v196, v196, v197
	s_waitcnt lgkmcnt(1)
	v_add_f32_e32 v196, v196, v200
	v_add_f32_e32 v200, v196, v201
	ds_read2_b32 v[196:197], v195 offset0:192 offset1:224
	s_waitcnt lgkmcnt(1)
	v_add_f32_e32 v202, v200, v202
	ds_read2_b32 v[200:201], v204 offset1:32
	v_add_f32_e32 v202, v202, v203
	s_waitcnt lgkmcnt(1)
	v_add_f32_e32 v196, v202, v196
	ds_read2_b32 v[202:203], v204 offset0:64 offset1:96
	v_add_f32_e32 v196, v196, v197
	s_waitcnt lgkmcnt(1)
	v_add_f32_e32 v200, v196, v200
	ds_read2_b32 v[196:197], v204 offset0:128 offset1:160
	v_add_f32_e32 v200, v200, v201
	s_waitcnt lgkmcnt(1)
	v_add_f32_e32 v200, v200, v202
	v_add_f32_e32 v202, v200, v203
	ds_read2_b32 v[200:201], v204 offset0:192 offset1:224
	v_add_u32_e32 v204, 0x800, v195
	s_waitcnt lgkmcnt(1)
	v_add_f32_e32 v196, v202, v196
	ds_read2_b32 v[202:203], v204 offset1:32
	v_add_f32_e32 v196, v196, v197
	s_waitcnt lgkmcnt(1)
	v_add_f32_e32 v200, v196, v200
	ds_read2_b32 v[196:197], v204 offset0:64 offset1:96
	v_add_f32_e32 v200, v200, v201
	s_waitcnt lgkmcnt(1)
	v_add_f32_e32 v202, v200, v202
	ds_read2_b32 v[200:201], v204 offset0:128 offset1:160
	v_add_f32_e32 v202, v202, v203
	s_waitcnt lgkmcnt(1)
	v_add_f32_e32 v196, v202, v196
	v_add_f32_e32 v202, v196, v197
	ds_read2_b32 v[196:197], v204 offset0:192 offset1:224
	v_add_u32_e32 v195, 0xc00, v195
	s_waitcnt lgkmcnt(1)
	v_add_f32_e32 v200, v202, v200
	ds_read2_b32 v[202:203], v195 offset1:32
	v_add_f32_e32 v200, v200, v201
	s_waitcnt lgkmcnt(1)
	v_add_f32_e32 v196, v200, v196
	v_add_f32_e32 v200, v196, v197
	ds_read2_b32 v[196:197], v195 offset0:64 offset1:96
	s_waitcnt lgkmcnt(1)
	v_add_f32_e32 v202, v200, v202
	ds_read2_b32 v[200:201], v195 offset0:128 offset1:160
	v_add_f32_e32 v204, v202, v203
	ds_read2_b32 v[202:203], v195 offset0:192 offset1:224
	s_waitcnt lgkmcnt(2)
	v_add_f32_e32 v195, v204, v196
	v_add_f32_e32 v195, v195, v197
	s_waitcnt lgkmcnt(1)
	v_add_f32_e32 v195, v195, v200
	v_add_f32_e32 v195, v195, v201
	s_waitcnt lgkmcnt(0)
	v_add_f32_e32 v195, v195, v202
	v_add_f32_e32 v195, v195, v203
	v_lshl_add_u32 v197, v198, 2, s26
	v_and_b32_e32 v196, 0x3fffffe0, v198
	ds_write_b32 v197, v195
	s_waitcnt lgkmcnt(0)
	v_lshl_add_u32 v196, v196, 2, s26
	ds_read_b128 v[200:203], v196
	ds_read_b128 v[204:207], v196 offset:16
	ds_read_b128 v[208:211], v196 offset:32
	ds_read_b128 v[222:225], v196 offset:48
	s_waitcnt lgkmcnt(3)
	v_cmp_eq_f32_e64 s[10:11], v200, v195
	v_cmp_gt_f32_e32 vcc, v200, v195
	s_and_b64 s[10:11], s[12:13], s[10:11]
	s_or_b64 s[10:11], vcc, s[10:11]
	v_cndmask_b32_e64 v197, 0, 1, s[10:11]
	v_cmp_eq_f32_e64 s[10:11], v201, v195
	v_cmp_lt_u32_e64 s[12:13], 1, v194
	v_cmp_gt_f32_e32 vcc, v201, v195
	s_and_b64 s[10:11], s[10:11], s[12:13]
	s_or_b64 vcc, vcc, s[10:11]
	v_addc_co_u32_e32 v197, vcc, 0, v197, vcc
	v_cmp_eq_f32_e64 s[10:11], v202, v195
	v_cmp_lt_u32_e64 s[12:13], 2, v194
	v_cmp_gt_f32_e32 vcc, v202, v195
	s_and_b64 s[10:11], s[10:11], s[12:13]
	s_or_b64 s[10:11], vcc, s[10:11]
	v_cndmask_b32_e64 v200, 0, 1, s[10:11]
	v_cmp_eq_f32_e64 s[10:11], v203, v195
	v_cmp_lt_u32_e64 s[12:13], 3, v194
	v_cmp_gt_f32_e32 vcc, v203, v195
	s_and_b64 s[10:11], s[10:11], s[12:13]
	s_or_b64 vcc, vcc, s[10:11]
	v_addc_co_u32_e32 v197, vcc, v197, v200, vcc
	s_waitcnt lgkmcnt(2)
	v_cmp_eq_f32_e64 s[10:11], v204, v195
	v_cmp_lt_u32_e64 s[12:13], 4, v194
	v_cmp_gt_f32_e32 vcc, v204, v195
	s_and_b64 s[10:11], s[10:11], s[12:13]
	s_or_b64 s[10:11], vcc, s[10:11]
	v_cndmask_b32_e64 v200, 0, 1, s[10:11]
	v_cmp_eq_f32_e64 s[10:11], v205, v195
	v_cmp_lt_u32_e64 s[12:13], 5, v194
	v_cmp_gt_f32_e32 vcc, v205, v195
	s_and_b64 s[10:11], s[10:11], s[12:13]
	s_or_b64 vcc, vcc, s[10:11]
	v_addc_co_u32_e32 v197, vcc, v197, v200, vcc
	v_cmp_eq_f32_e64 s[10:11], v206, v195
	v_cmp_lt_u32_e64 s[12:13], 6, v194
	v_cmp_gt_f32_e32 vcc, v206, v195
	s_and_b64 s[10:11], s[10:11], s[12:13]
	s_or_b64 s[10:11], vcc, s[10:11]
	v_cndmask_b32_e64 v200, 0, 1, s[10:11]
	v_cmp_eq_f32_e64 s[10:11], v207, v195
	v_cmp_lt_u32_e64 s[12:13], 7, v194
	v_cmp_gt_f32_e32 vcc, v207, v195
	s_and_b64 s[10:11], s[10:11], s[12:13]
	s_or_b64 vcc, vcc, s[10:11]
	v_addc_co_u32_e32 v197, vcc, v197, v200, vcc
	s_waitcnt lgkmcnt(1)
	v_cmp_eq_f32_e64 s[10:11], v208, v195
	v_cmp_lt_u32_e64 s[12:13], 8, v194
	v_cmp_gt_f32_e32 vcc, v208, v195
	s_and_b64 s[10:11], s[10:11], s[12:13]
	s_or_b64 s[10:11], vcc, s[10:11]
	v_cndmask_b32_e64 v200, 0, 1, s[10:11]
	v_cmp_eq_f32_e64 s[10:11], v209, v195
	v_cmp_lt_u32_e64 s[12:13], 9, v194
	v_cmp_gt_f32_e32 vcc, v209, v195
	s_and_b64 s[10:11], s[10:11], s[12:13]
	s_or_b64 vcc, vcc, s[10:11]
	v_addc_co_u32_e32 v197, vcc, v197, v200, vcc
	v_cmp_eq_f32_e64 s[10:11], v210, v195
	v_cmp_lt_u32_e64 s[12:13], 10, v194
	v_cmp_gt_f32_e32 vcc, v210, v195
	s_and_b64 s[10:11], s[10:11], s[12:13]
	s_or_b64 s[10:11], vcc, s[10:11]
	v_cndmask_b32_e64 v200, 0, 1, s[10:11]
	v_cmp_eq_f32_e64 s[10:11], v211, v195
	v_cmp_lt_u32_e64 s[12:13], 11, v194
	v_cmp_gt_f32_e32 vcc, v211, v195
	s_and_b64 s[10:11], s[10:11], s[12:13]
	s_or_b64 vcc, vcc, s[10:11]
	v_addc_co_u32_e32 v197, vcc, v197, v200, vcc
	s_waitcnt lgkmcnt(0)
	v_cmp_eq_f32_e64 s[10:11], v222, v195
	v_cmp_lt_u32_e64 s[12:13], 12, v194
	v_cmp_gt_f32_e32 vcc, v222, v195
	s_and_b64 s[10:11], s[10:11], s[12:13]
	s_or_b64 s[10:11], vcc, s[10:11]
	v_cndmask_b32_e64 v200, 0, 1, s[10:11]
	v_cmp_eq_f32_e64 s[10:11], v223, v195
	v_cmp_lt_u32_e64 s[12:13], 13, v194
	v_cmp_gt_f32_e32 vcc, v223, v195
	s_and_b64 s[10:11], s[10:11], s[12:13]
	s_or_b64 vcc, vcc, s[10:11]
	v_addc_co_u32_e32 v197, vcc, v197, v200, vcc
	v_cmp_eq_f32_e64 s[10:11], v224, v195
	v_cmp_lt_u32_e64 s[12:13], 14, v194
	v_cmp_gt_f32_e32 vcc, v224, v195
	s_and_b64 s[10:11], s[10:11], s[12:13]
	ds_read_b128 v[200:203], v196 offset:64
	s_or_b64 s[10:11], vcc, s[10:11]
	v_cndmask_b32_e64 v204, 0, 1, s[10:11]
	v_cmp_eq_f32_e64 s[10:11], v225, v195
	v_cmp_lt_u32_e64 s[12:13], 15, v194
	v_cmp_gt_f32_e32 vcc, v225, v195
	s_and_b64 s[10:11], s[10:11], s[12:13]
	s_or_b64 vcc, vcc, s[10:11]
	v_addc_co_u32_e32 v197, vcc, v197, v204, vcc
	ds_read_b128 v[204:207], v196 offset:80
	s_waitcnt lgkmcnt(1)
	v_cmp_eq_f32_e64 s[10:11], v200, v195
	v_cmp_lt_u32_e64 s[12:13], 16, v194
	v_cmp_gt_f32_e32 vcc, v200, v195
	s_and_b64 s[10:11], s[10:11], s[12:13]
	s_or_b64 s[10:11], vcc, s[10:11]
	v_cndmask_b32_e64 v200, 0, 1, s[10:11]
	v_cmp_eq_f32_e64 s[10:11], v201, v195
	v_cmp_lt_u32_e64 s[12:13], 17, v194
	v_cmp_gt_f32_e32 vcc, v201, v195
	s_and_b64 s[10:11], s[10:11], s[12:13]
	s_or_b64 vcc, vcc, s[10:11]
	v_addc_co_u32_e32 v197, vcc, v197, v200, vcc
	v_cmp_eq_f32_e64 s[10:11], v202, v195
	v_cmp_lt_u32_e64 s[12:13], 18, v194
	v_cmp_gt_f32_e32 vcc, v202, v195
	s_and_b64 s[10:11], s[10:11], s[12:13]
	s_or_b64 s[10:11], vcc, s[10:11]
	v_cndmask_b32_e64 v200, 0, 1, s[10:11]
	v_cmp_eq_f32_e64 s[10:11], v203, v195
	v_cmp_lt_u32_e64 s[12:13], 19, v194
	v_cmp_gt_f32_e32 vcc, v203, v195
	s_and_b64 s[10:11], s[10:11], s[12:13]
	s_or_b64 vcc, vcc, s[10:11]
	v_addc_co_u32_e32 v197, vcc, v197, v200, vcc
	s_waitcnt lgkmcnt(0)
	v_cmp_eq_f32_e64 s[10:11], v204, v195
	v_cmp_lt_u32_e64 s[12:13], 20, v194
	v_cmp_gt_f32_e32 vcc, v204, v195
	s_and_b64 s[10:11], s[10:11], s[12:13]
	s_or_b64 s[10:11], vcc, s[10:11]
	v_cndmask_b32_e64 v200, 0, 1, s[10:11]
	v_cmp_eq_f32_e64 s[10:11], v205, v195
	v_cmp_lt_u32_e64 s[12:13], 21, v194
	v_cmp_gt_f32_e32 vcc, v205, v195
	s_and_b64 s[10:11], s[10:11], s[12:13]
	s_or_b64 vcc, vcc, s[10:11]
	v_addc_co_u32_e32 v197, vcc, v197, v200, vcc
	v_cmp_eq_f32_e64 s[10:11], v206, v195
	v_cmp_lt_u32_e64 s[12:13], 22, v194
	v_cmp_gt_f32_e32 vcc, v206, v195
	s_and_b64 s[10:11], s[10:11], s[12:13]
	ds_read_b128 v[200:203], v196 offset:96
	s_or_b64 s[10:11], vcc, s[10:11]
	v_cndmask_b32_e64 v204, 0, 1, s[10:11]
	v_cmp_eq_f32_e64 s[10:11], v207, v195
	v_cmp_lt_u32_e64 s[12:13], 23, v194
	v_cmp_gt_f32_e32 vcc, v207, v195
	s_and_b64 s[10:11], s[10:11], s[12:13]
	s_or_b64 vcc, vcc, s[10:11]
	v_addc_co_u32_e32 v197, vcc, v197, v204, vcc
	ds_read_b128 v[204:207], v196 offset:112
	s_waitcnt lgkmcnt(1)
	v_cmp_eq_f32_e64 s[10:11], v200, v195
	v_cmp_lt_u32_e64 s[12:13], 24, v194
	v_cmp_gt_f32_e32 vcc, v200, v195
	s_and_b64 s[10:11], s[10:11], s[12:13]
	s_or_b64 s[10:11], vcc, s[10:11]
	v_cndmask_b32_e64 v196, 0, 1, s[10:11]
	v_cmp_eq_f32_e64 s[10:11], v201, v195
	v_cmp_lt_u32_e64 s[12:13], 25, v194
	v_cmp_gt_f32_e32 vcc, v201, v195
	s_and_b64 s[10:11], s[10:11], s[12:13]
	s_or_b64 vcc, vcc, s[10:11]
	v_addc_co_u32_e32 v196, vcc, v197, v196, vcc
	v_cmp_eq_f32_e64 s[10:11], v202, v195
	v_cmp_lt_u32_e64 s[12:13], 26, v194
	v_cmp_gt_f32_e32 vcc, v202, v195
	s_and_b64 s[10:11], s[10:11], s[12:13]
	s_or_b64 s[10:11], vcc, s[10:11]
	v_cndmask_b32_e64 v197, 0, 1, s[10:11]
	v_cmp_eq_f32_e64 s[10:11], v203, v195
	v_cmp_lt_u32_e64 s[12:13], 27, v194
	v_cmp_gt_f32_e32 vcc, v203, v195
	s_and_b64 s[10:11], s[10:11], s[12:13]
	s_or_b64 vcc, vcc, s[10:11]
	v_addc_co_u32_e32 v196, vcc, v196, v197, vcc
	s_waitcnt lgkmcnt(0)
	v_cmp_eq_f32_e64 s[10:11], v204, v195
	v_cmp_lt_u32_e64 s[12:13], 28, v194
	v_cmp_gt_f32_e32 vcc, v204, v195
	s_and_b64 s[10:11], s[10:11], s[12:13]
	s_or_b64 s[10:11], vcc, s[10:11]
	v_cndmask_b32_e64 v197, 0, 1, s[10:11]
	v_cmp_eq_f32_e64 s[10:11], v205, v195
	v_cmp_lt_u32_e64 s[12:13], 29, v194
	v_cmp_gt_f32_e32 vcc, v205, v195
	s_and_b64 s[10:11], s[10:11], s[12:13]
	s_or_b64 vcc, vcc, s[10:11]
	v_addc_co_u32_e32 v196, vcc, v196, v197, vcc
	v_cmp_eq_f32_e64 s[10:11], v206, v195
	v_cmp_eq_u32_e64 s[12:13], 31, v194
	v_cmp_gt_f32_e32 vcc, v206, v195
	s_and_b64 s[12:13], s[12:13], s[10:11]
	v_cmp_gt_f32_e64 s[10:11], v207, v195
	s_or_b64 vcc, vcc, s[12:13]
	s_nop 0
	v_cndmask_b32_e64 v197, 0, 1, s[10:11]
	v_addc_co_u32_e32 v196, vcc, v196, v197, vcc
	v_ashrrev_i32_e32 v197, 5, v198
	v_lshl_add_u32 v198, v197, 4, s27
	v_cmp_gt_u32_e32 vcc, 4, v196
	s_and_saveexec_b64 s[10:11], vcc
	v_lshl_add_u32 v200, v196, 2, v198
	ds_write_b32 v200, v195
	s_or_b64 exec, exec, s[10:11]
	s_waitcnt lgkmcnt(0)
	s_and_b64 exec, exec, vcc
	s_cbranch_execz .LBB0_1171
	ds_read_b128 v[200:203], v198
	s_waitcnt lgkmcnt(0)
	v_sub_f32_e32 v198, v201, v200
	v_sub_f32_e32 v201, v202, v200
	v_mul_f32_e32 v198, 0x3fb8aa3b, v198
	v_sub_f32_e32 v202, v203, v200
	v_mul_f32_e32 v201, 0x3fb8aa3b, v201
	v_exp_f32_e32 v198, v198
	v_mul_f32_e32 v202, 0x3fb8aa3b, v202
	v_exp_f32_e32 v201, v201
	v_sub_f32_e32 v195, v195, v200
	v_exp_f32_e32 v202, v202
	v_mul_f32_e32 v195, 0x3fb8aa3b, v195
	v_exp_f32_e32 v195, v195
	v_add_f32_e32 v198, 1.0, v198
	v_add_f32_e32 v198, v198, v201
	v_sub_u32_e32 v203, v220, v1
	v_add_f32_e32 v198, v198, v202
	v_add_u32_e32 v197, v203, v197
	v_div_scale_f32 v202, s[10:11], v198, v198, v195
	v_lshl_or_b32 v196, v197, 2, v196
	v_rcp_f32_e32 v203, v202
	v_ashrrev_i32_e32 v197, 31, v196
	v_lshlrev_b64 v[196:197], 2, v[196:197]
	v_lshl_add_u64 v[200:201], s[14:15], 0, v[196:197]
	global_store_dword v[200:201], v194, off
	v_fma_f32 v200, -v202, v203, 1.0
	v_fmac_f32_e32 v203, v200, v203
	v_div_scale_f32 v200, vcc, v195, v198, v195
	v_mul_f32_e32 v201, v200, v203
	v_fma_f32 v204, -v202, v201, v200
	v_fmac_f32_e32 v201, v204, v203
	v_fma_f32 v200, -v202, v201, v200
	v_div_fmas_f32 v200, v200, v203, v201
	v_div_fixup_f32 v195, v200, v198, v195
	v_lshl_add_u64 v[196:197], s[16:17], 0, v[196:197]
	v_lshl_add_u32 v194, v194, 2, 0
	global_store_dword v[196:197], v195, off
	v_add_u32_e32 v194, 0x18400, v194
	ds_add_u32 v194, v219
	s_branch .LBB0_1171
